# baseline (speedup 1.0000x reference)
.LBB0_89:
	v_mov_b32_e32 v112, v22
	v_mov_b32_e32 v113, v23
	v_mov_b32_e32 v114, v24
	v_mov_b32_e32 v115, v25
	v_mov_b32_e32 v3, 0
	v_lshlrev_b32_e32 v70, 4, v28
	s_and_saveexec_b64 s[60:61], vcc
	s_cbranch_execz .LBB0_118
	s_mov_b64 s[92:93], s[14:15]
	v_lshl_add_u64 v[22:23], s[12:13], 0, v[2:3]
	s_waitcnt vmcnt(0)
	v_cndmask_b32_e64 v55, -1, v4, s[0:1]
	s_movk_i32 s0, 0x880
	v_mov_b32_e32 v2, 0x1dd00
	v_mad_u32_u24 v4, v80, s0, v2
	v_lshlrev_b32_e32 v2, 1, v1
	v_mov_b32_e32 v27, v3
	v_mbcnt_hi_u32_b32 v2, -1, v29
	v_lshl_add_u64 v[72:73], v[22:23], 0, v[26:27]
	v_and_b32_e32 v23, 64, v2
	v_xor_b32_e32 v22, 16, v2
	v_add_u32_e32 v23, 64, v23
	v_cmp_lt_i32_e32 vcc, v22, v23
	v_lshlrev_b32_e32 v88, 2, v28
	v_and_b32_e32 v24, 7, v0
	v_cndmask_b32_e32 v22, v2, v22, vcc
	v_lshlrev_b32_e32 v90, 2, v22
	v_xor_b32_e32 v22, 32, v2
	v_cmp_lt_i32_e32 vcc, v22, v23
	s_mov_b32 s24, 0x10000
	v_cndmask_b32_e32 v2, v2, v22, vcc
	v_lshlrev_b32_e32 v91, 2, v2
	v_lshrrev_b32_e32 v2, 2, v79
	v_mul_u32_u24_e32 v22, 0x88, v79
	v_add3_u32 v92, v4, v22, v1
	v_or_b32_e32 v2, v88, v2
	v_lshlrev_b32_e32 v22, 3, v0
	v_mul_u32_u24_e32 v2, 0x88, v2
	v_and_b32_e32 v22, 24, v22
	v_add3_u32 v93, v4, v2, v22
	v_lshlrev_b32_e32 v2, 5, v24
	v_or3_b32 v78, v2, v1, s24
	v_bfe_u32 v2, v0, 1, 2
	v_lshrrev_b32_e32 v89, 3, v79
	v_cmp_eq_u32_e64 s[6:7], 4, v24
	v_cmp_eq_u32_e64 s[8:9], 3, v24
	v_cmp_eq_u32_e64 s[10:11], 2, v24
	v_cmp_eq_u32_e64 s[12:13], 1, v24
	v_cmp_eq_u32_e64 s[14:15], 0, v24
	v_cmp_eq_u32_e64 s[16:17], 7, v24
	v_cmp_eq_u32_e64 s[18:19], 6, v24
	v_cmp_eq_u32_e64 s[20:21], 5, v24
	v_cmp_eq_u32_e64 s[22:23], 0, v2
	v_cmp_eq_u32_e64 s[24:25], 1, v2
	v_cmp_eq_u32_e64 s[26:27], 2, v2
	v_cmp_eq_u32_e64 s[28:29], 3, v2
	s_and_b64 s[22:23], s[22:23], s[4:5]
	s_and_b64 s[24:25], s[24:25], s[4:5]
	s_and_b64 s[26:27], s[26:27], s[4:5]
	s_and_b64 s[28:29], s[28:29], s[4:5]
	v_mov_b32_e32 v71, 0xf149f2ca
	s_mov_b64 s[62:63], 0
	s_mov_b32 s69, 0xf149f2ca
	s_mov_b32 s70, 0xefa18f08
	s_mov_b32 s71, 0x41000000
	s_movk_i32 s72, 0x110
	s_mov_b32 s77, 0x26500
	s_mov_b32 s73, 0x2650c
	s_mov_b32 s80, -1
	s_mov_b32 s81, 0
	s_mov_b32 s82, 0
	s_mov_b32 s83, 0x7fffffff
	s_mov_b64 s[84:85], 0
	v_mov_b32_e32 v100, 0
	v_mov_b32_e32 v4, 0
	v_mov_b32_e32 v103, 0xf149f2ca
	v_mov_b32_e32 v46, v3
	v_mov_b32_e32 v47, v3
	v_mov_b32_e32 v48, v3
	v_mov_b32_e32 v49, v3
	v_mov_b32_e32 v50, v3
	v_mov_b32_e32 v51, v3
	v_mov_b32_e32 v52, v3
	v_mov_b32_e32 v53, v3
	v_mov_b32_e32 v38, v3
	v_mov_b32_e32 v39, v3
	v_mov_b32_e32 v40, v3
	v_mov_b32_e32 v41, v3
	v_mov_b32_e32 v42, v3
	v_mov_b32_e32 v43, v3
	v_mov_b32_e32 v44, v3
	v_mov_b32_e32 v45, v3
	v_mov_b32_e32 v30, v3
	v_mov_b32_e32 v31, v3
	v_mov_b32_e32 v32, v3
	v_mov_b32_e32 v33, v3
	v_mov_b32_e32 v34, v3
	v_mov_b32_e32 v35, v3
	v_mov_b32_e32 v36, v3
	v_mov_b32_e32 v37, v3
	v_mov_b32_e32 v22, v3
	v_mov_b32_e32 v23, v3
	v_mov_b32_e32 v24, v3
	v_mov_b32_e32 v25, v3
	v_mov_b32_e32 v26, v3
	v_mov_b32_e32 v28, v3
	v_mov_b32_e32 v29, v3
	v_readfirstlane_b32 s86, v80
	s_mov_b32 s87, 0
	v_readfirstlane_b32 s88, v99
	v_readfirstlane_b32 s89, v5
	v_readfirstlane_b32 s96, v54
	v_readfirstlane_b32 s97, v84
	v_readfirstlane_b32 s98, v85
	v_readfirstlane_b32 s99, v81
	v_readfirstlane_b32 s100, v83
	v_readfirstlane_b32 s101, v82
	v_mov_b32_e32 v84, v82
	s_cmp_ge_i32 s96, s68
	s_cselect_b32 s100, 0, s100
	s_branch .LBB0_95

.Lattn_T:
	ds_read_b128 v[4:7], v86
	ds_read_b128 v[8:11], v86 offset:1024
	ds_read_b128 v[12:15], v86 offset:4096
	ds_read_b128 v[22:25], v86 offset:5120
	ds_read_b128 v[34:37], v86 offset:2048
	ds_read_b128 v[38:41], v86 offset:3072
	ds_read_b128 v[42:45], v86 offset:6144
	ds_read_b128 v[46:49], v86 offset:7168
	v_cndmask_b32_e64 v21, 0, v102, s[22:23]
	v_cndmask_b32_e64 v20, 0, v101, s[22:23]
	v_cndmask_b32_e64 v19, 0, v100, s[22:23]
	v_cndmask_b32_e64 v18, 0, v99, s[22:23]
	v_cndmask_b32_e64 v29, 0, v102, s[24:25]
	v_cndmask_b32_e64 v28, 0, v101, s[24:25]
	v_cndmask_b32_e64 v27, 0, v100, s[24:25]
	v_cndmask_b32_e64 v26, 0, v99, s[24:25]
	v_cndmask_b32_e64 v33, 0, v102, s[26:27]
	v_cndmask_b32_e64 v32, 0, v101, s[26:27]
	v_cndmask_b32_e64 v31, 0, v100, s[26:27]
	v_cndmask_b32_e64 v30, 0, v99, s[26:27]
	v_cndmask_b32_e64 v53, 0, v102, s[28:29]
	v_cndmask_b32_e64 v52, 0, v101, s[28:29]
	v_cndmask_b32_e64 v51, 0, v100, s[28:29]
	v_cndmask_b32_e64 v50, 0, v99, s[28:29]
	s_waitcnt lgkmcnt(7)
	v_mfma_f32_16x16x32_f16 v[4:7], v[4:7], v[18:21], 0
	s_waitcnt lgkmcnt(5)
	v_mfma_f32_16x16x32_f16 v[12:15], v[12:15], v[18:21], 0
	v_mfma_f32_16x16x32_f16 v[4:7], v[8:11], v[26:29], v[4:7]
	s_waitcnt lgkmcnt(4)
	v_mfma_f32_16x16x32_f16 v[8:11], v[22:25], v[26:29], v[12:15]
	s_nop 4
	ds_read_b128 v[12:15], v86 offset:13312
	ds_read_b128 v[22:25], v86 offset:12288
	ds_read_b128 v[54:57], v86 offset:9216
	ds_read_b128 v[58:61], v86 offset:8192
	s_waitcnt lgkmcnt(7)
	v_mfma_f32_16x16x32_f16 v[4:7], v[34:37], v[30:33], v[4:7]
	s_waitcnt lgkmcnt(5)
	v_mfma_f32_16x16x32_f16 v[8:11], v[42:45], v[30:33], v[8:11]
	s_waitcnt lgkmcnt(4)
	v_mfma_f32_16x16x32_f16 v[34:37], v[46:49], v[50:53], v[8:11]
	v_mfma_f32_16x16x32_f16 v[4:7], v[38:41], v[50:53], v[4:7]
	s_nop 6
	v_cvt_pk_f16_f32 v9, v36, v37
	v_cvt_pk_f16_f32 v8, v34, v35
	v_cvt_pk_f16_f32 v7, v6, v7
	v_cvt_pk_f16_f32 v6, v4, v5
	ds_read_b128 v[34:37], v86 offset:10240
	ds_read_b128 v[38:41], v86 offset:11264
	ds_read_b128 v[42:45], v86 offset:14336
	ds_read_b128 v[46:49], v86 offset:15360
	s_waitcnt lgkmcnt(6)
	v_mfma_f32_16x16x32_f16 v[22:25], v[22:25], v[18:21], 0
	s_waitcnt lgkmcnt(4)
	v_mfma_f32_16x16x32_f16 v[58:61], v[58:61], v[18:21], 0
	v_mfma_f32_16x16x32_f16 v[10:13], v[12:15], v[26:29], v[22:25]
	v_mfma_f32_16x16x32_f16 v[54:57], v[54:57], v[26:29], v[58:61]
	ds_read_b128 v[14:17], v86 offset:21504
	s_nop 2
	ds_read_b128 v[22:25], v86 offset:20480
	s_nop 0
	ds_read_b128 v[58:61], v86 offset:17408
	ds_read_b128 v[62:65], v86 offset:16384
	s_waitcnt lgkmcnt(7)
	v_mfma_f32_16x16x32_f16 v[34:37], v[34:37], v[30:33], v[54:57]
	s_waitcnt lgkmcnt(5)
	v_mfma_f32_16x16x32_f16 v[10:13], v[42:45], v[30:33], v[10:13]
	s_waitcnt lgkmcnt(4)
	v_mfma_f32_16x16x32_f16 v[10:13], v[46:49], v[50:53], v[10:13]
	v_mfma_f32_16x16x32_f16 v[34:37], v[38:41], v[50:53], v[34:37]
	s_nop 6
	v_cvt_pk_f16_f32 v13, v12, v13
	v_cvt_pk_f16_f32 v12, v10, v11
	v_cvt_pk_f16_f32 v11, v36, v37
	v_cvt_pk_f16_f32 v10, v34, v35
	ds_read_b128 v[34:37], v86 offset:18432
	ds_read_b128 v[38:41], v86 offset:19456
	ds_read_b128 v[42:45], v86 offset:22528
	ds_read_b128 v[46:49], v86 offset:23552
	s_waitcnt lgkmcnt(6)
	v_mfma_f32_16x16x32_f16 v[22:25], v[22:25], v[18:21], 0
	s_waitcnt lgkmcnt(4)
	v_mfma_f32_16x16x32_f16 v[54:57], v[62:65], v[18:21], 0
	v_mfma_f32_16x16x32_f16 v[14:17], v[14:17], v[26:29], v[22:25]
	v_mfma_f32_16x16x32_f16 v[54:57], v[58:61], v[26:29], v[54:57]
	s_nop 3
	ds_read_b128 v[22:25], v86 offset:29696
	ds_read_b128 v[58:61], v86 offset:28672
	ds_read_b128 v[62:65], v86 offset:25600
	ds_read_b128 v[66:69], v86 offset:24576
	s_waitcnt lgkmcnt(7)
	v_mfma_f32_16x16x32_f16 v[34:37], v[34:37], v[30:33], v[54:57]
	s_waitcnt lgkmcnt(5)
	v_mfma_f32_16x16x32_f16 v[14:17], v[42:45], v[30:33], v[14:17]
	s_waitcnt lgkmcnt(4)
	v_mfma_f32_16x16x32_f16 v[14:17], v[46:49], v[50:53], v[14:17]
	v_mfma_f32_16x16x32_f16 v[34:37], v[38:41], v[50:53], v[34:37]
	s_nop 6
	v_cvt_pk_f16_f32 v17, v16, v17
	v_cvt_pk_f16_f32 v16, v14, v15
	v_cvt_pk_f16_f32 v15, v36, v37
	v_cvt_pk_f16_f32 v14, v34, v35
	ds_read_b128 v[34:37], v86 offset:26624
	ds_read_b128 v[38:41], v86 offset:27648
	ds_read_b128 v[42:45], v86 offset:30720
	ds_read_b128 v[46:49], v86 offset:31744
	s_waitcnt lgkmcnt(4)
	v_mfma_f32_16x16x32_f16 v[54:57], v[66:69], v[18:21], 0
	v_mfma_f32_16x16x32_f16 v[18:21], v[58:61], v[18:21], 0
	v_mfma_f32_16x16x32_f16 v[18:21], v[22:25], v[26:29], v[18:21]
	v_mfma_f32_16x16x32_f16 v[54:57], v[62:65], v[26:29], v[54:57]
	s_waitcnt lgkmcnt(3)
	v_mfma_f32_16x16x32_f16 v[22:25], v[34:37], v[30:33], v[54:57]
	s_waitcnt lgkmcnt(1)
	v_mfma_f32_16x16x32_f16 v[18:21], v[42:45], v[30:33], v[18:21]
	s_waitcnt lgkmcnt(0)
	v_mfma_f32_16x16x32_f16 v[18:21], v[46:49], v[50:53], v[18:21]
	v_mfma_f32_16x16x32_f16 v[22:25], v[38:41], v[50:53], v[22:25]
	s_nop 6
	v_cvt_pk_f16_f32 v21, v20, v21
	v_cvt_pk_f16_f32 v20, v18, v19
	v_cvt_pk_f16_f32 v19, v24, v25
	v_cvt_pk_f16_f32 v18, v22, v23

.Lattn_k0:
	v_mov_b32_e32 v99, v112
	v_mov_b32_e32 v100, v113
	v_mov_b32_e32 v101, v114
	v_mov_b32_e32 v102, v115
	s_mov_b64 s[0:1], exec
	s_mov_b64 s[40:41], exec
	s_branch .Lattn_T
